# attention-phase conversion jobs in step-major order (all workgroups sweep one contiguous 16 MB window of the f32 weights per step) for DRAM locality
# speedup vs baseline: 1.0100x; 1.0100x over previous
; #define LAS __attribute__((address_space(3)))
; __device__ __forceinline__ void moba_attn_unit(const Args& a, LAS unsigned char* lds, int bh, int qb, int half, int cjob0) {
;     ...
;     const int nown = 2 * half + 2, nsteps = (nown + 4 * qb) >> 1;
;     bf16x8 qf[2][4]; unsigned sm[2]; float m[2], l[2]; f32x4 O[8][2];
; #pragma unroll
;     for (int b2 = 0; b2 < 2; ++b2) { const size_t qrow = (size_t)bh * SEQ + qb * 256 + qbase + 16 * b2 + fr;
; #pragma unroll
;         for (int ks = 0; ks < 4; ++ks) qf[b2][ks] = *(const bf16x8*)(qbr + qrow * 128 + ks * 32 + 8 * g);
;         sm[b2] = sel[qrow]; m[b2] = -INFINITY; l[b2] = 0.f;
; #pragma unroll
;         for (int dt = 0; dt < 8; ++dt) O[dt][b2] = (f32x4){0.f, 0.f, 0.f, 0.f}; }
;     const float cs = 0.08838834764831845f * 1.4426950408889634f;
;     unsigned kso[2], vso[2];
; #pragma unroll
;     for (int p = 0; p < 2; ++p) { const int kr = 4 * (w + 8 * p) + (lane >> 4), kc = (lane & 15) ^ (kr & 15); kso[p] = (unsigned)(kr * 256 + kc * 16);
;         const int vr = 8 * (w + 8 * p) + (lane >> 3), vc = (lane & 7) ^ ((vr >> 1) & 7); vso[p] = (unsigned)(vr * (SEQ * 2) + vc * 16); }
;     const char* kbase = (const char*)(kbr + (size_t)bh * SEQ * 128); const char* vbase = (const char*)(vbt + (size_t)bh * 128 * SEQ);
;     auto tile_jk = [&](int ti, int& j, int& kt) { if (ti < nown) { j = qb; kt = ti; } else { const int tj = ti - nown; j = tj >> 2; kt = tj & 3; } };
;     auto stage = [&](int s) {
; #pragma unroll
;         for (int t2 = 0; t2 < 2; ++t2) { int j, kt; tile_jk(2 * s + t2, j, kt); const int key0 = j * 256 + kt * 64;
;             LAS unsigned char* dstb = lds + (s & 1) * 65536 + t2 * 32768 + w * 1024;
;             const char* ks = pg8::sbase(kbase + (size_t)key0 * 256); const char* vs = pg8::sbase(vbase + (size_t)key0 * 2);
; #pragma unroll
;             for (int p = 0; p < 2; ++p) {
;                 __builtin_amdgcn_global_load_lds((const unsigned*)(ks + kso[p]), (LAS unsigned*)(dstb + p * 8192), 16, 0, 0);
;                 __builtin_amdgcn_global_load_lds((const unsigned*)(vs + vso[p]), (LAS unsigned*)(dstb + 16384 + p * 8192), 16, 0, 0); } } };
;     __syncthreads();
;     stage(0);
;     f32x4 cv[8]; const int cjob = __builtin_amdgcn_readfirstlane(cjob0);
;     if (CONV_IN_ATTN) { const SJob cj = sjob_addr(a, cjob, lane); sjob_load(cj, cv); }
.LBB0_430:
	s_ashr_i32 s39, s38, 4
	s_sub_i32 s0, 31, s39
	s_and_b32 s54, s38, 15
	s_lshr_b32 s24, s0, 1
	s_and_b32 s10, s0, 1
	s_lshl_b32 s0, s24, 8
	v_lshl_or_b32 v2, s54, 12, v166
	s_lshl_b32 s2, s54, 20
	v_lshl_or_b32 v165, s10, 7, v181
	v_add_u32_e32 v2, s0, v2
	s_add_u32 s25, s3, s2
	v_or_b32_e32 v2, v2, v165
	v_mov_b32_e32 v3, v169
	s_addc_u32 s28, s20, 0
	s_mov_b32 s1, s13
	v_lshlrev_b64 v[4:5], 8, v[2:3]
	s_add_u32 s29, s21, s2
	v_lshl_add_u64 v[4:5], v[182:183], 0, v[4:5]
	s_addc_u32 s30, s22, 0
	s_lshl_b64 s[8:9], s[0:1], 8
	global_load_dwordx4 v[66:69], v[4:5], off
	global_load_dwordx4 v[70:73], v[4:5], off offset:64
	global_load_dwordx4 v[74:77], v[4:5], off offset:128
	global_load_dwordx4 v[78:81], v[4:5], off offset:192
	v_lshl_add_u64 v[4:5], v[2:3], 2, s[14:15]
	v_or_b32_e32 v2, 16, v2
	s_add_u32 s8, s25, s8
	v_lshlrev_b64 v[6:7], 8, v[2:3]
	s_addc_u32 s9, s28, s9
	s_lshl_b32 s1, s24, 9
	v_lshl_add_u64 v[6:7], v[182:183], 0, v[6:7]
	v_lshl_add_u64 v[2:3], v[2:3], 2, s[14:15]
	s_add_u32 s16, s29, s1
	v_readfirstlane_b32 s1, v189
	global_load_dword v187, v[4:5], off
	global_load_dwordx4 v[82:85], v[6:7], off
	global_load_dwordx4 v[86:89], v[6:7], off offset:64
	global_load_dwordx4 v[90:93], v[6:7], off offset:128
	global_load_dwordx4 v[94:97], v[6:7], off offset:192
	global_load_dword v215, v[2:3], off
	s_waitcnt vmcnt(0)
	s_barrier
	s_addc_u32 s17, s30, 0
	v_lshl_add_u64 v[2:3], s[8:9], 0, v[170:171]
	s_mov_b32 m0, s1
	v_readfirstlane_b32 s1, v204
	global_load_lds_dwordx4 v[2:3], off
	v_lshl_add_u64 v[2:3], s[16:17], 0, v[172:173]
	s_mov_b32 m0, s1
	s_or_b32 s12, s0, 64
	global_load_lds_dwordx4 v[2:3], off
	v_lshl_add_u64 v[2:3], s[8:9], 0, v[174:175]
	v_readfirstlane_b32 s1, v205
	s_lshl_b64 s[8:9], s[12:13], 8
	s_mov_b32 m0, s1
	v_readfirstlane_b32 s1, v206
	s_add_u32 s8, s25, s8
	global_load_lds_dwordx4 v[2:3], off
	s_mov_b32 m0, s1
	s_addc_u32 s9, s28, s9
	s_lshl_b32 s1, s12, 1
	v_lshl_add_u64 v[2:3], s[16:17], 0, v[176:177]
	s_add_u32 s16, s29, s1
	v_readfirstlane_b32 s1, v207
	global_load_lds_dwordx4 v[2:3], off
	s_addc_u32 s17, s30, 0
	v_lshl_add_u64 v[2:3], s[8:9], 0, v[170:171]
	s_mov_b32 m0, s1
	v_readfirstlane_b32 s1, v208
	global_load_lds_dwordx4 v[2:3], off
	v_lshl_add_u64 v[2:3], s[16:17], 0, v[172:173]
	s_mov_b32 m0, s1
	v_readfirstlane_b32 s1, v209
	global_load_lds_dwordx4 v[2:3], off
	v_lshl_add_u64 v[2:3], s[8:9], 0, v[174:175]
	s_mov_b32 m0, s1
	v_readfirstlane_b32 s1, v210
	global_load_lds_dwordx4 v[2:3], off
	v_lshl_add_u64 v[2:3], s[16:17], 0, v[176:177]
	s_mov_b32 m0, s1
	s_lshl_b32 s1, s38, 3
	global_load_lds_dwordx4 v[2:3], off
	v_or_b32_e32 v186, s1, v167
	s_mov_b64 s[8:9], -1
	v_readfirstlane_b32 s1, v186
	s_cmp_gt_i32 s1, 0x1ffff
	s_cbranch_scc0 .LBB0_432
	s_and_b32 s2, s1, 0x7fffffc0
	s_add_i32 s2, s2, 0xfffe0000
	v_or_b32_e32 v2, s2, v178
	v_mov_b32_e32 v3, v169
	v_lshlrev_b64 v[2:3], 13, v[2:3]
	s_lshl_b32 s31, s1, 5
	v_lshl_add_u64 v[2:3], s[50:51], 0, v[2:3]
	s_and_b32 s12, s31, 0x7e0
	s_mov_b64 s[8:9], 0

; __device__ __forceinline__ void moba_attn_unit(const Args& a, LAS unsigned char* lds, int bh, int qb, int half, int cjob0) {
;     ...
; #pragma unroll 1
;     for (int s = 0; s < nsteps; ++s) {
;         asm volatile("s_waitcnt vmcnt(0)" ::: "memory");
;         __syncthreads();
;         if (s + 1 < nsteps) stage(s + 1);
;         if (CONV_IN_ATTN) { { const SJob cj = sjob_addr(a, cjob + 8 * s, lane); sjob_store(cj, cv); } if (s + 1 < nsteps) { const SJob cn = sjob_addr(a, cjob + 8 * (s + 1), lane); sjob_load(cn, cv); } }
.LBB0_436:
	s_or_b64 exec, exec, s[16:17]
	s_add_i32 s56, s56, 0x10000
	s_add_i32 s58, s58, 2
	s_add_i32 s1, s1, 0x800
	s_add_i32 s31, s31, 0x10000
	s_add_i32 s55, s55, 0x20000
	s_cmp_eq_u32 s53, s59
	s_cbranch_scc1 .LBB0_462

; __device__ __forceinline__ unsigned pk4_fp8_scaled(float a, float b, float c, float d) { s16x2 r = {0, 0}; r = __builtin_amdgcn_cvt_scalef32_pk_fp8_f32(r, a, b, pg8::W8_INV, false); r = __builtin_amdgcn_cvt_scalef32_pk_fp8_f32(r, c, d, pg8::W8_INV, true); return __builtin_bit_cast(unsigned, r); }
; __device__ __forceinline__ SJob sjob_addr(const Args& a, int j, int lane) {
;     SJob c; const int kseg = lane & 7, nq = lane >> 3;
;     if (j < SJOBS_GU) { const int e = j >> 12, kb = (j >> 7) & 31, nb = j & 127, s0 = nb * 32, bj = s0 >> 11, rem = s0 & 2047, pn = rem >> 7, c0 = rem & 127, np = pn * 256 + bj * 128 + c0;
;         c.ld = 4096; c.src = a.w_gate_up + ((size_t)e * 2048 + kb * 64 + kseg * 8) * 4096 + s0 + nq * 4; c.dst = (unsigned char*)(a.ws + WS_WGU_T) + ((size_t)e * 4096 + np + nq * 4) * 2048 + kb * 64 + kseg * 8; }
;     else { const int jj = j - SJOBS_GU, e = jj >> 11, kb = (jj >> 6) & 31, nb = jj & 63;
;         c.ld = 2048; c.src = a.w_down + ((size_t)e * 2048 + kb * 64 + kseg * 8) * 2048 + nb * 32 + nq * 4; c.dst = (unsigned char*)(a.ws + WS_WD_T) + ((size_t)e * 2048 + nb * 32 + nq * 4) * 2048 + kb * 64 + kseg * 8; }
;     return c;
; }
; __device__ __forceinline__ void sjob_load(const SJob& c, f32x4 (&v)[8]) {
; #pragma unroll
;     for (int r = 0; r < 8; ++r) v[r] = __builtin_nontemporal_load((const f32x4*)(c.src + (size_t)r * c.ld));
; }
; __device__ __forceinline__ void sjob_store(const SJob& c, const f32x4 (&v)[8]) {
; #pragma unroll
;     for (int jn = 0; jn < 4; ++jn) { u32x2 o;
;         o.x = pk4_fp8_scaled(v[0][jn], v[1][jn], v[2][jn], v[3][jn]); o.y = pk4_fp8_scaled(v[4][jn], v[5][jn], v[6][jn], v[7][jn]);
;         __builtin_nontemporal_store(o, (u32x2*)(c.dst + (size_t)jn * 2048)); }
; }
; __device__ __forceinline__ void moba_attn_unit(const Args& a, LAS unsigned char* lds, int bh, int qb, int half, int cjob0) {
;     ...
;         if (CONV_IN_ATTN) { { const SJob cj = sjob_addr(a, cjob + 8 * s, lane); sjob_store(cj, cv); } if (s + 1 < nsteps) { const SJob cn = sjob_addr(a, cjob + 8 * (s + 1), lane); sjob_load(cn, cv); } }
.LBB0_441:
	s_add_u32 s10, s74, s10
	s_addc_u32 s11, s75, s11
	v_lshlrev_b64 v[130:131], 11, v[130:131]
	s_and_b32 s12, s12, 0x7c0
	v_lshl_add_u64 v[130:131], s[10:11], 0, v[130:131]
	v_mov_b32_e32 v132, 0
	v_mov_b32_e32 v133, 0
	v_lshl_add_u64 v[130:131], v[130:131], 0, s[12:13]
	v_cvt_scalef32_pk_fp8_f32 v132, v98, v102, s23
	v_cvt_scalef32_pk_fp8_f32 v133, v114, v118, s23
	v_lshl_add_u64 v[130:131], v[130:131], 0, v[178:179]
	v_cvt_scalef32_pk_fp8_f32 v132, v106, v110, s23 op_sel:[0,0,0,1]
	v_cvt_scalef32_pk_fp8_f32 v133, v122, v126, s23 op_sel:[0,0,0,1]
	global_store_dwordx2 v[130:131], v[132:133], off nt
	v_mov_b32_e32 v132, 0
	v_mov_b32_e32 v133, 0
	v_cvt_scalef32_pk_fp8_f32 v132, v99, v103, s23
	v_cvt_scalef32_pk_fp8_f32 v133, v115, v119, s23
	v_cvt_scalef32_pk_fp8_f32 v132, v107, v111, s23 op_sel:[0,0,0,1]
	v_cvt_scalef32_pk_fp8_f32 v133, v123, v127, s23 op_sel:[0,0,0,1]
	global_store_dwordx2 v[130:131], v[132:133], off offset:2048 nt
	v_mov_b32_e32 v132, 0
	v_mov_b32_e32 v133, 0
	v_cvt_scalef32_pk_fp8_f32 v132, v100, v104, s23
	v_cvt_scalef32_pk_fp8_f32 v133, v116, v120, s23
	v_add_co_u32_e32 v130, vcc, 0x1000, v130
	v_cvt_scalef32_pk_fp8_f32 v132, v108, v112, s23 op_sel:[0,0,0,1]
	v_cvt_scalef32_pk_fp8_f32 v133, v124, v128, s23 op_sel:[0,0,0,1]
	v_addc_co_u32_e32 v131, vcc, 0, v131, vcc
	global_store_dwordx2 v[130:131], v[132:133], off nt
	v_mov_b32_e32 v132, 0
	v_mov_b32_e32 v133, 0
	v_cvt_scalef32_pk_fp8_f32 v132, v101, v105, s23
	v_cvt_scalef32_pk_fp8_f32 v133, v117, v121, s23
	v_cvt_scalef32_pk_fp8_f32 v132, v109, v113, s23 op_sel:[0,0,0,1]
	v_cvt_scalef32_pk_fp8_f32 v133, v125, v129, s23 op_sel:[0,0,0,1]
	s_andn2_b64 vcc, exec, s[8:9]
	global_store_dwordx2 v[130:131], v[132:133], off offset:2048 nt
	s_cbranch_vccnz .LBB0_447
	s_add_i32 s10, s1, 0x800
	s_cmp_gt_i32 s10, 0x1ffff
	s_mov_b64 s[8:9], -1
	s_cbranch_scc0 .LBB0_444
	s_and_b32 s2, s10, 0x7fffffc0
	s_add_i32 s2, s2, 0xfffe0000
	v_or_b32_e32 v98, s2, v178
	v_mov_b32_e32 v99, v169
	v_lshlrev_b64 v[98:99], 13, v[98:99]
	s_add_i32 s2, s31, 0x10000
	v_lshl_add_u64 v[98:99], s[50:51], 0, v[98:99]
	s_and_b32 s12, s2, 0x7e0
	s_mov_b64 s[8:9], 0
.LBB0_444:
	s_andn2_b64 vcc, exec, s[8:9]
	s_mov_b64 s[8:9], 0x800
	s_cbranch_vccnz .LBB0_446
	s_ashr_i32 s8, s10, 12
	s_add_i32 s2, s31, 0x10000
	s_and_b32 s12, s2, 0xfe0
	s_ashr_i32 s9, s8, 31
	s_lshr_b32 s2, s10, 1
	s_lshl_b64 s[8:9], s[8:9], 11
	s_and_b32 s2, s2, 0x7c0
	s_or_b32 s2, s8, s2
	v_mov_b32_e32 v99, s9
	v_or_b32_e32 v98, s2, v178
	v_lshlrev_b64 v[98:99], 14, v[98:99]
	v_lshl_add_u64 v[98:99], s[46:47], 0, v[98:99]
	s_mov_b64 s[8:9], 0x1000

; #define LAS __attribute__((address_space(3)))
; __device__ __forceinline__ void moba_attn_unit(const Args& a, LAS unsigned char* lds, int bh, int qb, int half, int cjob0) {
;     ...
;     const int nown = 2 * half + 2, nsteps = (nown + 4 * qb) >> 1;
;     bf16x8 qf[2][4]; unsigned sm[2]; float m[2], l[2]; f32x4 O[8][2];
; #pragma unroll
;     for (int b2 = 0; b2 < 2; ++b2) { const size_t qrow = (size_t)bh * SEQ + qb * 256 + qbase + 16 * b2 + fr;
; #pragma unroll
;         for (int ks = 0; ks < 4; ++ks) qf[b2][ks] = *(const bf16x8*)(qbr + qrow * 128 + ks * 32 + 8 * g);
;         sm[b2] = sel[qrow]; m[b2] = -INFINITY; l[b2] = 0.f;
; #pragma unroll
;         for (int dt = 0; dt < 8; ++dt) O[dt][b2] = (f32x4){0.f, 0.f, 0.f, 0.f}; }
;     const float cs = 0.08838834764831845f * 1.4426950408889634f;
;     unsigned kso[2], vso[2];
; #pragma unroll
;     for (int p = 0; p < 2; ++p) { const int kr = 4 * (w + 8 * p) + (lane >> 4), kc = (lane & 15) ^ (kr & 15); kso[p] = (unsigned)(kr * 256 + kc * 16);
;         const int vr = 8 * (w + 8 * p) + (lane >> 3), vc = (lane & 7) ^ ((vr >> 1) & 7); vso[p] = (unsigned)(vr * (SEQ * 2) + vc * 16); }
;     const char* kbase = (const char*)(kbr + (size_t)bh * SEQ * 128); const char* vbase = (const char*)(vbt + (size_t)bh * 128 * SEQ);
;     auto tile_jk = [&](int ti, int& j, int& kt) { if (ti < nown) { j = qb; kt = ti; } else { const int tj = ti - nown; j = tj >> 2; kt = tj & 3; } };
;     auto stage = [&](int s) {
; #pragma unroll
;         for (int t2 = 0; t2 < 2; ++t2) { int j, kt; tile_jk(2 * s + t2, j, kt); const int key0 = j * 256 + kt * 64;
;             LAS unsigned char* dstb = lds + (s & 1) * 65536 + t2 * 32768 + w * 1024;
;             const char* ks = pg8::sbase(kbase + (size_t)key0 * 256); const char* vs = pg8::sbase(vbase + (size_t)key0 * 2);
; #pragma unroll
;             for (int p = 0; p < 2; ++p) {
;                 __builtin_amdgcn_global_load_lds((const unsigned*)(ks + kso[p]), (LAS unsigned*)(dstb + p * 8192), 16, 0, 0);
;                 __builtin_amdgcn_global_load_lds((const unsigned*)(vs + vso[p]), (LAS unsigned*)(dstb + 16384 + p * 8192), 16, 0, 0); } } };
;     __syncthreads();
;     stage(0);
;     f32x4 cv[8]; const int cjob = __builtin_amdgcn_readfirstlane(cjob0);
;     if (CONV_IN_ATTN) { const SJob cj = sjob_addr(a, cjob, lane); sjob_load(cj, cv); }
.LBB0_466:
	s_or_b64 exec, exec, s[8:9]
	s_sub_i32 s0, 0x1ff, s38
	s_lshl_b32 s2, s39, 11
	s_and_b32 s39, s0, 15
	s_lshr_b32 s0, s0, 4
	s_sub_i32 s0, 31, s0
	s_ashr_i32 s24, s0, 1
	s_and_b32 s10, s0, 1
	s_lshl_b32 s0, s24, 8
	s_ashr_i32 s1, s0, 31
	v_lshl_or_b32 v2, s39, 12, v166
	v_mov_b32_e32 v3, v1
	s_lshl_b32 s8, s39, 20
	v_lshl_or_b32 v187, s10, 7, v181
	v_lshl_add_u64 v[2:3], v[2:3], 0, s[0:1]
	s_add_u32 s25, s3, s8
	v_or_b32_e32 v2, v2, v187
	s_addc_u32 s28, s20, 0
	v_lshlrev_b64 v[4:5], 8, v[2:3]
	s_add_u32 s29, s21, s8
	v_lshl_add_u64 v[4:5], v[182:183], 0, v[4:5]
	s_addc_u32 s30, s22, 0
	s_lshl_b64 s[8:9], s[0:1], 8
	s_barrier
	global_load_dwordx4 v[70:73], v[4:5], off
	global_load_dwordx4 v[74:77], v[4:5], off offset:64
	global_load_dwordx4 v[78:81], v[4:5], off offset:128
	global_load_dwordx4 v[82:85], v[4:5], off offset:192
	v_lshl_add_u64 v[4:5], v[2:3], 2, s[14:15]
	v_or_b32_e32 v2, 16, v2
	s_add_u32 s8, s25, s8
	v_lshlrev_b64 v[6:7], 8, v[2:3]
	s_addc_u32 s9, s28, s9
	s_lshl_b64 s[16:17], s[0:1], 1
	v_lshl_add_u64 v[6:7], v[182:183], 0, v[6:7]
	v_lshl_add_u64 v[2:3], v[2:3], 2, s[14:15]
	s_add_u32 s16, s29, s16
	v_readfirstlane_b32 s1, v189
	global_load_dword v35, v[4:5], off
	global_load_dwordx4 v[86:89], v[6:7], off
	global_load_dwordx4 v[90:93], v[6:7], off offset:64
	global_load_dwordx4 v[94:97], v[6:7], off offset:128
	global_load_dwordx4 v[98:101], v[6:7], off offset:192
	global_load_dword v216, v[2:3], off
	s_barrier
	s_addc_u32 s17, s30, s17
	v_lshl_add_u64 v[2:3], s[8:9], 0, v[170:171]
	s_mov_b32 m0, s1
	v_readfirstlane_b32 s1, v204
	global_load_lds_dwordx4 v[2:3], off
	v_lshl_add_u64 v[2:3], s[16:17], 0, v[172:173]
	s_mov_b32 m0, s1
	v_readfirstlane_b32 s1, v205
	global_load_lds_dwordx4 v[2:3], off
	v_lshl_add_u64 v[2:3], s[8:9], 0, v[174:175]
	s_or_b32 s8, s0, 64
	s_mov_b32 m0, s1
	s_ashr_i32 s9, s8, 31
	global_load_lds_dwordx4 v[2:3], off
	v_lshl_add_u64 v[2:3], s[16:17], 0, v[176:177]
	s_lshl_b64 s[16:17], s[8:9], 8
	s_add_u32 s16, s25, s16
	v_readfirstlane_b32 s1, v206
	s_addc_u32 s17, s28, s17
	s_lshl_b64 s[8:9], s[8:9], 1
	s_mov_b32 m0, s1
	s_add_u32 s8, s29, s8
	v_readfirstlane_b32 s1, v207
	global_load_lds_dwordx4 v[2:3], off
	s_addc_u32 s9, s30, s9
	v_lshl_add_u64 v[2:3], s[16:17], 0, v[170:171]
	s_mov_b32 m0, s1
	v_readfirstlane_b32 s1, v208
	global_load_lds_dwordx4 v[2:3], off
	v_lshl_add_u64 v[2:3], s[8:9], 0, v[172:173]
	s_mov_b32 m0, s1
	v_readfirstlane_b32 s1, v209
	global_load_lds_dwordx4 v[2:3], off
	v_lshl_add_u64 v[2:3], s[16:17], 0, v[174:175]
	s_mov_b32 m0, s1
	v_readfirstlane_b32 s1, v210
	global_load_lds_dwordx4 v[2:3], off
	v_lshl_add_u64 v[2:3], s[8:9], 0, v[176:177]
	s_mov_b32 m0, s1
	s_mov_b64 s[8:9], -1
	global_load_lds_dwordx4 v[2:3], off
	v_subrev_u32_e32 v2, s2, v186
	s_nop 0
	v_readfirstlane_b32 s11, v2
	s_add_i32 s1, s11, 0x10000
	s_cmp_gt_i32 s1, 0x1ffff
	s_cbranch_scc0 .LBB0_468
	s_and_b32 s2, s1, 0x7fffffc0
	s_add_i32 s2, s2, 0xfffe0000
	v_or_b32_e32 v2, s2, v178
	v_mov_b32_e32 v3, v169
	v_lshlrev_b64 v[2:3], 13, v[2:3]
	s_lshl_b32 s2, s11, 5
	v_lshl_add_u64 v[2:3], s[50:51], 0, v[2:3]
	s_and_b32 s12, s2, 0x7e0
	s_mov_b64 s[8:9], 0

; #define LAS __attribute__((address_space(3)))
; __device__ __forceinline__ void moba_attn_unit(const Args& a, LAS unsigned char* lds, int bh, int qb, int half, int cjob0) {
;     ...
;     const int nown = 2 * half + 2, nsteps = (nown + 4 * qb) >> 1;
;     bf16x8 qf[2][4]; unsigned sm[2]; float m[2], l[2]; f32x4 O[8][2];
; #pragma unroll
;     for (int b2 = 0; b2 < 2; ++b2) { const size_t qrow = (size_t)bh * SEQ + qb * 256 + qbase + 16 * b2 + fr;
; #pragma unroll
;         for (int ks = 0; ks < 4; ++ks) qf[b2][ks] = *(const bf16x8*)(qbr + qrow * 128 + ks * 32 + 8 * g);
;         sm[b2] = sel[qrow]; m[b2] = -INFINITY; l[b2] = 0.f;
; #pragma unroll
;         for (int dt = 0; dt < 8; ++dt) O[dt][b2] = (f32x4){0.f, 0.f, 0.f, 0.f}; }
;     const float cs = 0.08838834764831845f * 1.4426950408889634f;
;     unsigned kso[2], vso[2];
; #pragma unroll
;     for (int p = 0; p < 2; ++p) { const int kr = 4 * (w + 8 * p) + (lane >> 4), kc = (lane & 15) ^ (kr & 15); kso[p] = (unsigned)(kr * 256 + kc * 16);
;         const int vr = 8 * (w + 8 * p) + (lane >> 3), vc = (lane & 7) ^ ((vr >> 1) & 7); vso[p] = (unsigned)(vr * (SEQ * 2) + vc * 16); }
;     const char* kbase = (const char*)(kbr + (size_t)bh * SEQ * 128); const char* vbase = (const char*)(vbt + (size_t)bh * 128 * SEQ);
;     auto tile_jk = [&](int ti, int& j, int& kt) { if (ti < nown) { j = qb; kt = ti; } else { const int tj = ti - nown; j = tj >> 2; kt = tj & 3; } };
;     auto stage = [&](int s) {
; #pragma unroll
;         for (int t2 = 0; t2 < 2; ++t2) { int j, kt; tile_jk(2 * s + t2, j, kt); const int key0 = j * 256 + kt * 64;
;             LAS unsigned char* dstb = lds + (s & 1) * 65536 + t2 * 32768 + w * 1024;
;             const char* ks = pg8::sbase(kbase + (size_t)key0 * 256); const char* vs = pg8::sbase(vbase + (size_t)key0 * 2);
; #pragma unroll
;             for (int p = 0; p < 2; ++p) {
;                 __builtin_amdgcn_global_load_lds((const unsigned*)(ks + kso[p]), (LAS unsigned*)(dstb + p * 8192), 16, 0, 0);
;                 __builtin_amdgcn_global_load_lds((const unsigned*)(vs + vso[p]), (LAS unsigned*)(dstb + 16384 + p * 8192), 16, 0, 0); } } };
;     __syncthreads();
;     stage(0);
;     f32x4 cv[8]; const int cjob = __builtin_amdgcn_readfirstlane(cjob0);
;     if (CONV_IN_ATTN) { const SJob cj = sjob_addr(a, cjob, lane); sjob_load(cj, cv); }
.LBB0_470:
	s_lshl_b32 s31, s10, 1
	s_add_i32 s33, s31, 2
	s_lshl_b32 s2, s24, 2
	s_add_i32 s2, s33, s2
	s_ashr_i32 s52, s2, 1
	s_cmp_lt_i32 s52, 1
	s_mov_b32 s53, 0
	s_cbranch_scc1 .LBB0_499
	v_lshl_add_u64 v[2:3], s[12:13], 2, v[2:3]
	v_lshl_add_u64 v[2:3], v[2:3], 0, v[168:169]
	s_lshl_b32 s12, s8, 2
	v_lshl_add_u64 v[4:5], v[2:3], 0, s[12:13]
	global_load_dwordx4 v[102:105], v[2:3], off nt
	global_load_dwordx4 v[106:109], v[4:5], off nt
	v_lshl_add_u64 v[2:3], v[4:5], 0, s[12:13]
	v_lshl_add_u64 v[4:5], v[2:3], 0, s[12:13]
	global_load_dwordx4 v[110:113], v[2:3], off nt
	global_load_dwordx4 v[114:117], v[4:5], off nt
	v_lshl_add_u64 v[2:3], v[4:5], 0, s[12:13]
	v_lshl_add_u64 v[4:5], v[2:3], 0, s[12:13]
	global_load_dwordx4 v[118:121], v[2:3], off nt
	global_load_dwordx4 v[122:125], v[4:5], off nt
	v_lshl_add_u64 v[2:3], v[4:5], 0, s[12:13]
	v_lshl_add_u64 v[4:5], v[2:3], 0, s[12:13]
	global_load_dwordx4 v[126:129], v[2:3], off nt
	global_load_dwordx4 v[130:133], v[4:5], off nt
	s_lshl_b32 s2, s11, 5
	v_mov_b32_e32 v10, v169
	v_mov_b32_e32 v11, v169
	v_mov_b32_e32 v12, v169
	v_mov_b32_e32 v13, v169
	v_or_b32_e32 v219, v187, v166
	s_add_i32 s54, s2, 0x200000
	s_lshl_b32 s2, s11, 6
	v_mov_b64_e32 v[48:49], v[12:13]
	v_mov_b64_e32 v[16:17], v[12:13]
	v_mov_b64_e32 v[52:53], v[12:13]
	v_mov_b64_e32 v[20:21], v[12:13]
	v_mov_b64_e32 v[56:57], v[12:13]
	v_mov_b64_e32 v[24:25], v[12:13]
	v_mov_b64_e32 v[60:61], v[12:13]
	v_mov_b64_e32 v[28:29], v[12:13]
	v_mov_b64_e32 v[64:65], v[12:13]
	v_mov_b64_e32 v[32:33], v[12:13]
	v_mov_b64_e32 v[68:69], v[12:13]
	v_mov_b64_e32 v[44:45], v[12:13]
	v_mov_b64_e32 v[6:7], v[10:11]
	v_mov_b64_e32 v[40:41], v[12:13]
	v_mov_b64_e32 v[2:3], v[10:11]
	v_or_b32_e32 v218, 31, v187
	v_or_b32_e32 v220, 16, v219
	v_add_u32_e32 v221, 14, v219
	v_add_u32_e32 v222, 13, v219
	v_subrev_u32_e32 v223, s31, v188
	s_add_i32 s55, s2, 0x400000
	s_sub_i32 s56, 0, s31
	v_mov_b32_e32 v217, 0xff800000
	v_mov_b32_e32 v186, 0
	s_mov_b32 s57, 3
	v_mov_b64_e32 v[46:47], v[10:11]
	v_mov_b64_e32 v[14:15], v[10:11]
	v_mov_b64_e32 v[50:51], v[10:11]
	v_mov_b64_e32 v[18:19], v[10:11]
	v_mov_b64_e32 v[54:55], v[10:11]
	v_mov_b64_e32 v[22:23], v[10:11]
	v_mov_b64_e32 v[58:59], v[10:11]
	v_mov_b64_e32 v[26:27], v[10:11]
	v_mov_b64_e32 v[62:63], v[10:11]
	v_mov_b64_e32 v[30:31], v[10:11]
	v_mov_b64_e32 v[66:67], v[10:11]
	v_mov_b64_e32 v[42:43], v[10:11]
	v_mov_b64_e32 v[8:9], v[12:13]
	v_mov_b64_e32 v[38:39], v[10:11]
	v_mov_b64_e32 v[4:5], v[12:13]
	v_mov_b32_e32 v34, 0
	v_mov_b32_e32 v215, 0xff800000
	s_mov_b32 s58, 0
	s_branch .LBB0_474

; __device__ __forceinline__ void moba_attn_unit(const Args& a, LAS unsigned char* lds, int bh, int qb, int half, int cjob0) {
;     ...
; #pragma unroll 1
;     for (int s = 0; s < nsteps; ++s) {
;         asm volatile("s_waitcnt vmcnt(0)" ::: "memory");
;         __syncthreads();
;         if (s + 1 < nsteps) stage(s + 1);
;         if (CONV_IN_ATTN) { { const SJob cj = sjob_addr(a, cjob + 8 * s, lane); sjob_store(cj, cv); } if (s + 1 < nsteps) { const SJob cn = sjob_addr(a, cjob + 8 * (s + 1), lane); sjob_load(cn, cv); } }
.LBB0_473:
	s_or_b64 exec, exec, s[16:17]
	s_add_i32 s53, s53, 0x10000
	s_add_i32 s57, s57, 2
	s_add_i32 s1, s1, 0x800
	s_add_i32 s54, s54, 0x10000
	s_add_i32 s55, s55, 0x20000
	s_cmp_eq_u32 s52, s58
	s_cbranch_scc1 .LBB0_500

; __device__ __forceinline__ unsigned pk4_fp8_scaled(float a, float b, float c, float d) { s16x2 r = {0, 0}; r = __builtin_amdgcn_cvt_scalef32_pk_fp8_f32(r, a, b, pg8::W8_INV, false); r = __builtin_amdgcn_cvt_scalef32_pk_fp8_f32(r, c, d, pg8::W8_INV, true); return __builtin_bit_cast(unsigned, r); }
; __device__ __forceinline__ SJob sjob_addr(const Args& a, int j, int lane) {
;     SJob c; const int kseg = lane & 7, nq = lane >> 3;
;     if (j < SJOBS_GU) { const int e = j >> 12, kb = (j >> 7) & 31, nb = j & 127, s0 = nb * 32, bj = s0 >> 11, rem = s0 & 2047, pn = rem >> 7, c0 = rem & 127, np = pn * 256 + bj * 128 + c0;
;         c.ld = 4096; c.src = a.w_gate_up + ((size_t)e * 2048 + kb * 64 + kseg * 8) * 4096 + s0 + nq * 4; c.dst = (unsigned char*)(a.ws + WS_WGU_T) + ((size_t)e * 4096 + np + nq * 4) * 2048 + kb * 64 + kseg * 8; }
;     else { const int jj = j - SJOBS_GU, e = jj >> 11, kb = (jj >> 6) & 31, nb = jj & 63;
;         c.ld = 2048; c.src = a.w_down + ((size_t)e * 2048 + kb * 64 + kseg * 8) * 2048 + nb * 32 + nq * 4; c.dst = (unsigned char*)(a.ws + WS_WD_T) + ((size_t)e * 2048 + nb * 32 + nq * 4) * 2048 + kb * 64 + kseg * 8; }
;     return c;
; }
; __device__ __forceinline__ void sjob_load(const SJob& c, f32x4 (&v)[8]) {
; #pragma unroll
;     for (int r = 0; r < 8; ++r) v[r] = __builtin_nontemporal_load((const f32x4*)(c.src + (size_t)r * c.ld));
; }
; __device__ __forceinline__ void sjob_store(const SJob& c, const f32x4 (&v)[8]) {
; #pragma unroll
;     for (int jn = 0; jn < 4; ++jn) { u32x2 o;
;         o.x = pk4_fp8_scaled(v[0][jn], v[1][jn], v[2][jn], v[3][jn]); o.y = pk4_fp8_scaled(v[4][jn], v[5][jn], v[6][jn], v[7][jn]);
;         __builtin_nontemporal_store(o, (u32x2*)(c.dst + (size_t)jn * 2048)); }
; }
; __device__ __forceinline__ void moba_attn_unit(const Args& a, LAS unsigned char* lds, int bh, int qb, int half, int cjob0) {
;     ...
;         if (CONV_IN_ATTN) { { const SJob cj = sjob_addr(a, cjob + 8 * s, lane); sjob_store(cj, cv); } if (s + 1 < nsteps) { const SJob cn = sjob_addr(a, cjob + 8 * (s + 1), lane); sjob_load(cn, cv); } }
.LBB0_478:
	s_add_u32 s10, s74, s10
	s_addc_u32 s11, s75, s11
	v_lshlrev_b64 v[36:37], 11, v[36:37]
	s_and_b32 s12, s12, 0x7c0
	v_lshl_add_u64 v[36:37], s[10:11], 0, v[36:37]
	v_mov_b32_e32 v134, 0
	v_mov_b32_e32 v135, 0
	v_lshl_add_u64 v[36:37], v[36:37], 0, s[12:13]
	v_cvt_scalef32_pk_fp8_f32 v134, v102, v106, s23
	v_cvt_scalef32_pk_fp8_f32 v135, v118, v122, s23
	v_lshl_add_u64 v[36:37], v[36:37], 0, v[178:179]
	v_cvt_scalef32_pk_fp8_f32 v134, v110, v114, s23 op_sel:[0,0,0,1]
	v_cvt_scalef32_pk_fp8_f32 v135, v126, v130, s23 op_sel:[0,0,0,1]
	global_store_dwordx2 v[36:37], v[134:135], off nt
	v_mov_b32_e32 v134, 0
	v_mov_b32_e32 v135, 0
	v_cvt_scalef32_pk_fp8_f32 v134, v103, v107, s23
	v_cvt_scalef32_pk_fp8_f32 v135, v119, v123, s23
	v_cvt_scalef32_pk_fp8_f32 v134, v111, v115, s23 op_sel:[0,0,0,1]
	v_cvt_scalef32_pk_fp8_f32 v135, v127, v131, s23 op_sel:[0,0,0,1]
	global_store_dwordx2 v[36:37], v[134:135], off offset:2048 nt
	v_mov_b32_e32 v134, 0
	v_mov_b32_e32 v135, 0
	v_cvt_scalef32_pk_fp8_f32 v134, v104, v108, s23
	v_cvt_scalef32_pk_fp8_f32 v135, v120, v124, s23
	v_add_co_u32_e32 v36, vcc, 0x1000, v36
	v_cvt_scalef32_pk_fp8_f32 v134, v112, v116, s23 op_sel:[0,0,0,1]
	v_cvt_scalef32_pk_fp8_f32 v135, v128, v132, s23 op_sel:[0,0,0,1]
	v_addc_co_u32_e32 v37, vcc, 0, v37, vcc
	global_store_dwordx2 v[36:37], v[134:135], off nt
	v_mov_b32_e32 v134, 0
	v_mov_b32_e32 v135, 0
	v_cvt_scalef32_pk_fp8_f32 v134, v105, v109, s23
	v_cvt_scalef32_pk_fp8_f32 v135, v121, v125, s23
	v_cvt_scalef32_pk_fp8_f32 v134, v113, v117, s23 op_sel:[0,0,0,1]
	v_cvt_scalef32_pk_fp8_f32 v135, v129, v133, s23 op_sel:[0,0,0,1]
	s_andn2_b64 vcc, exec, s[8:9]
	global_store_dwordx2 v[36:37], v[134:135], off offset:2048 nt
	s_cbranch_vccnz .LBB0_484
	s_add_i32 s10, s1, 0x800
	s_cmp_gt_i32 s10, 0x1ffff
	s_mov_b64 s[8:9], -1
	s_cbranch_scc0 .LBB0_481
	s_and_b32 s2, s10, 0x7fffffc0
	s_add_i32 s2, s2, 0xfffe0000
	v_or_b32_e32 v36, s2, v178
	v_mov_b32_e32 v37, v169
	v_lshlrev_b64 v[36:37], 13, v[36:37]
	s_add_i32 s2, s54, 0x10000
	v_lshl_add_u64 v[36:37], s[50:51], 0, v[36:37]
	s_and_b32 s12, s2, 0x7e0
	s_mov_b64 s[8:9], 0
.LBB0_481:
	s_andn2_b64 vcc, exec, s[8:9]
	s_mov_b64 s[8:9], 0x800
	s_cbranch_vccnz .LBB0_483
	s_ashr_i32 s8, s10, 12
	s_add_i32 s2, s54, 0x10000
	s_and_b32 s12, s2, 0xfe0
	s_ashr_i32 s9, s8, 31
	s_lshr_b32 s2, s10, 1
	s_lshl_b64 s[8:9], s[8:9], 11
	s_and_b32 s2, s2, 0x7c0
	s_or_b32 s2, s8, s2
	v_mov_b32_e32 v37, s9
	v_or_b32_e32 v36, s2, v178
	v_lshlrev_b64 v[36:37], 14, v[36:37]
	v_lshl_add_u64 v[36:37], s[46:47], 0, v[36:37]
	s_mov_b64 s[8:9], 0x1000
